# mLSTM chunk top: vmcnt(0) skipped when the previous chunk finished a conversion tile (only its output stores are still in flight)
# speedup vs baseline: 1.0026x; 1.0026x over previous
; #define LAS __attribute__((address_space(3)))
; __device__ __forceinline__ int lane_id_() { int l; asm volatile("v_mbcnt_lo_u32_b32 %0, -1, 0\n\tv_mbcnt_hi_u32_b32 %0, -1, %0" : "=v"(l)); return l; }
; __device__ __forceinline__ void mlstm_unit(LAS unsigned char* lds, const bf16_t* __restrict__ PM, const float* __restrict__ GATES, bf16_t* __restrict__ Hout,
;                                            int b, int h, int dir, int vs, Conv& cvs, const int wave_) {
;     f32x4 cv[16];
;     const int w = wave_, lane = lane_id_(), tid = w * 64 + lane, g = lane >> 4, i16 = lane & 15, q4 = i16 >> 2, p4 = lane & 3;
;     const int sr = tid >> 3, c8 = tid & 7;
;     f32x4 accC[2][4];
; #pragma unroll
;     for (int a = 0; a < 2; ++a)
; #pragma unroll
;         for (int v = 0; v < 4; ++v) accC[a][v] = (f32x4){0.f, 0.f, 0.f, 0.f};
;     if (tid < 256) *(LAS float*)(lds + NV + tid * 4) = 0.f;
;     float m_in = 0.f;
;     bool pend_b = false;
;     u32x4 rq[4], rk[4], rv; float g_i = 0.f, g_f = 0.f;
;     const int gi_col = (dir ? 8 : 0) + h, gf_col = (dir ? 12 : 4) + h;
;     ...
;     ML_LOAD(0);
; #pragma unroll 1
;     for (int ci = 0; ci < 36; ++ci) {
.LBB0_538:
	s_and_b64 s[2:3], s[6:7], exec
	s_cselect_b32 s2, s67, s69
	s_cselect_b32 s3, s66, s68
	s_movk_i32 s31, 0x90
	s_add_i32 s8, 0, 0x10800
	s_lshl_b32 s77, s0, 11
	v_lshlrev_b32_e32 v24, 13, v21
	s_add_i32 s22, 0, 0x15000
	s_lshl_b32 s82, s78, 1
	v_mul_lo_u32 v29, v155, s31
	v_and_b32_e32 v160, 0xe000, v24
	v_lshlrev_b32_e32 v24, 1, v21
	s_add_u32 s3, s3, s82
	v_and_b32_e32 v26, 15, v21
	v_bfe_u32 v27, v21, 2, 2
	v_ashrrev_i32_e32 v25, 4, v21
	v_add_u32_e32 v30, s8, v29
	v_cmp_eq_u32_e64 s[8:9], 0, v21
	v_and_b32_e32 v146, -16, v24
	v_lshlrev_b32_e32 v24, 2, v21
	v_and_b32_e32 v37, -16, v21
	v_readlane_b32 s12, v255, 42
	v_lshlrev_b32_e32 v21, 3, v21
	s_addc_u32 s2, s2, 0
	v_readlane_b32 s13, v255, 31
	v_lshl_add_u32 v162, v26, 2, s12
	v_and_b32_e32 v21, 24, v21
	v_readlane_b32 s12, v255, 33
	s_add_u32 s3, s3, s80
	v_and_b32_e32 v148, 28, v24
	v_add_u32_e32 v163, s12, v21
	s_addc_u32 s12, s2, 0
	s_lshl_b32 s2, s13, 1
	v_lshlrev_b32_e32 v24, 2, v25
	s_add_u32 s2, s3, s2
	v_lshlrev_b32_e32 v39, 3, v25
	s_addc_u32 s3, s12, 0
	v_ashrrev_i32_e32 v25, 31, v24
	v_lshl_add_u64 v[150:151], v[24:25], 1, s[2:3]
	v_readlane_b32 s2, v255, 29
	v_readlane_b32 s15, v255, 41
	v_add_u32_e32 v38, s13, v24
	v_add_u32_e32 v24, s2, v21
	v_readlane_b32 s2, v255, 30
	v_add_u32_e32 v164, s15, v21
	v_readlane_b32 s3, v255, 36
	v_add_u32_e32 v21, s2, v39
	v_readlane_b32 s2, v255, 34
	v_or_b32_e32 v166, s3, v26
	v_add_u32_e32 v35, s15, v29
	v_or_b32_e32 v165, s2, v26
	v_cmp_le_i32_e32 vcc, v38, v165
	v_or_b32_e32 v36, s13, v26
	v_cmp_gt_u32_e64 s[12:13], s14, v20
	v_cndmask_b32_e64 v43, 0, 1, vcc
	v_cmp_ge_i32_e32 vcc, v38, v165
	s_movk_i32 s30, 0x210
	v_readlane_b32 s2, v255, 35
	v_cndmask_b32_e64 v44, 0, 1, vcc
	v_cndmask_b32_e64 v43, v44, v43, s[6:7]
	v_or_b32_e32 v44, 1, v38
	v_cmp_lt_i32_e32 vcc, v38, v165
	v_and_b32_e32 v43, 1, v43
	v_cmp_eq_u32_e64 s[14:15], 1, v43
	v_cndmask_b32_e64 v45, 0, 1, vcc
	v_cmp_ge_i32_e32 vcc, v44, v165
	v_lshlrev_b32_e32 v43, 2, v38
	v_mad_u32_u24 v36, v36, s30, v37
	v_cndmask_b32_e64 v46, 0, 1, vcc
	v_cndmask_b32_e64 v45, v46, v45, s[6:7]
	v_or_b32_e32 v46, 2, v38
	v_cmp_le_i32_e32 vcc, v46, v165
	v_and_b32_e32 v45, 1, v45
	v_cmp_eq_u32_e64 s[16:17], 1, v45
	v_cndmask_b32_e64 v47, 0, 1, vcc
	v_cmp_ge_i32_e32 vcc, v46, v165
	v_lshlrev_b32_e32 v45, 2, v44
	v_mul_u32_u24_e32 v51, 0x210, v26
	v_cndmask_b32_e64 v48, 0, 1, vcc
	v_cndmask_b32_e64 v47, v48, v47, s[6:7]
	v_or_b32_e32 v48, 3, v38
	v_cmp_le_i32_e32 vcc, v48, v165
	v_readlane_b32 s10, v255, 32
	v_lshlrev_b32_e32 v23, 3, v22
	v_cndmask_b32_e64 v49, 0, 1, vcc
	v_cmp_ge_i32_e32 vcc, v48, v165
	v_add_u32_e32 v161, s10, v39
	v_lshlrev_b32_e32 v40, 6, v22
	v_cndmask_b32_e64 v50, 0, 1, vcc
	v_cmp_le_i32_e32 vcc, v38, v166
	v_cndmask_b32_e64 v49, v50, v49, s[6:7]
	v_or_b32_e32 v50, s2, v26
	v_cndmask_b32_e64 v52, 0, 1, vcc
	v_cmp_ge_i32_e32 vcc, v38, v166
	s_add_i32 s2, 0, 0x8400
	v_add_u32_e32 v174, s2, v36
	v_cndmask_b32_e64 v53, 0, 1, vcc
	v_cmp_lt_i32_e32 vcc, v38, v166
	v_readlane_b32 s2, v255, 37
	v_lshlrev_b32_e32 v41, 7, v22
	v_cndmask_b32_e64 v38, 0, 1, vcc
	v_cmp_ge_i32_e32 vcc, v44, v166
	v_cmp_eq_u32_e64 s[10:11], 0, v22
	v_or_b32_e32 v22, v39, v27
	v_cndmask_b32_e64 v44, 0, 1, vcc
	v_cndmask_b32_e64 v38, v44, v38, s[6:7]
	v_and_b32_e32 v38, 1, v38
	v_cmp_le_i32_e32 vcc, v46, v166
	v_cmp_eq_u32_e64 s[24:25], 1, v38
	v_add_u32_e32 v39, 32, v39
	v_cndmask_b32_e64 v38, 0, 1, vcc
	v_cmp_ge_i32_e32 vcc, v46, v166
	v_mul_lo_u32 v28, v155, s30
	v_lshlrev_b32_e32 v34, 2, v20
	v_cndmask_b32_e64 v44, 0, 1, vcc
	v_cndmask_b32_e64 v38, v44, v38, s[6:7]
	v_and_b32_e32 v38, 1, v38
	v_cmp_le_i32_e32 vcc, v48, v166
	v_cmp_eq_u32_e64 s[26:27], 1, v38
	v_and_b32_e32 v25, 0xff, v20
	v_cndmask_b32_e64 v38, 0, 1, vcc
	v_cmp_ge_i32_e32 vcc, v48, v166
	v_cndmask_b32_e64 v20, v149, v153, s[12:13]
	v_and_b32_e32 v47, 1, v47
	v_cndmask_b32_e64 v44, 0, 1, vcc
	v_cndmask_b32_e64 v38, v44, v38, s[6:7]
	v_add_u32_e32 v44, s3, v26
	v_mad_u32_u24 v26, v26, s30, v37
	v_add_u32_e32 v176, s2, v26
	v_readlane_b32 s2, v255, 38
	v_and_b32_e32 v49, 1, v49
	v_mul_lo_u32 v169, v22, s31
	v_add_u32_e32 v177, s2, v26
	v_lshrrev_b32_e32 v26, 5, v155
	s_movk_i32 s2, 0x4200
	v_or_b32_e32 v27, v39, v27
	v_cndmask_b32_e64 v52, v53, v52, s[6:7]
	v_and_b32_e32 v38, 1, v38
	v_add_u32_e32 v178, 0, v36
	v_mul_lo_u32 v36, v26, s2
	v_add_u32_e32 v159, 0, v28
	v_add_u32_e32 v31, 0, v144
	v_lshlrev_b32_e32 v32, 2, v155
	v_lshlrev_b32_e32 v33, 2, v145
	v_add_u32_e32 v29, s22, v29
	v_add_u32_e32 v20, 0, v20
	v_lshlrev_b32_e32 v42, 2, v25
	v_cmp_eq_u32_e64 s[18:19], 1, v47
	v_lshlrev_b32_e32 v47, 2, v46
	v_cmp_eq_u32_e64 s[20:21], 1, v49
	v_lshlrev_b32_e32 v49, 2, v48
	v_mul_lo_u32 v27, v27, s31
	v_lshl_add_u32 v171, v39, 1, s22
	v_mul_lo_u32 v22, v22, s30
	v_add_u32_e32 v39, 0x1200, v169
	v_and_b32_e32 v52, 1, v52
	v_cmp_eq_u32_e64 s[28:29], 1, v38
	v_mul_lo_u32 v38, v166, s31
	v_mul_lo_u32 v44, v44, s30
	v_lshl_or_b32 v25, v25, 1, v36
	v_lshlrev_b32_e32 v140, 1, v23
	v_add_u32_e32 v23, 0, v41
	s_mov_b32 s0, 0
	v_ashrrev_i32_e32 v147, 31, v146
	v_lshlrev_b32_e32 v167, 2, v165
	v_mul_lo_u32 v168, v165, s31
	v_add_u32_e32 v170, s22, v37
	v_lshlrev_b32_e32 v172, 2, v166
	v_cmp_eq_u32_e64 s[22:23], 1, v52
	v_mul_lo_u32 v173, v50, s31
	v_add3_u32 v175, v44, v37, 0
	v_add_u32_e32 v179, 0x8400, v25
	v_lshlrev_b32_e32 v181, 7, v26
	s_mov_b64 s[30:31], 0
	s_mov_b64 s[92:93], 0
	v_add_u32_e32 v182, v30, v144
	v_add_u32_e32 v183, v31, v28
	v_add_u32_e32 v184, 0, v33
	v_add_u32_e32 v185, v35, v144
	s_lshl_b32 s78, s36, 1
	s_lshl_b32 s88, s35, 2
	s_lshl_b32 s90, s34, 2
	v_add_u32_e32 v186, v161, v38
	v_add_u32_e32 v187, v29, v144
	v_add_u32_e32 v188, v159, v40
	v_add_u32_e32 v189, 0x1f800, v23
	v_add_u32_e32 v190, v163, v27
	v_add_u32_e32 v191, v24, v22
	v_add_u32_e32 v192, v164, v39
	v_add_u32_e32 v193, v21, v51
	v_add_u32_e32 v194, v20, v42
	v_add_u32_e32 v195, 0, v34
	v_add_u32_e32 v196, 0, v32
	v_add_u32_e32 v197, 0, v43
	v_add_u32_e32 v198, 0, v45
	v_add_u32_e32 v199, 0, v47
	v_add_u32_e32 v200, 0, v49
	v_mov_b32_e32 v60, 0
	v_mov_b32_e32 v61, v156
	v_mov_b32_e32 v62, v156
	v_mov_b32_e32 v63, v156
	v_mov_b32_e32 v56, 0
	v_mov_b32_e32 v57, v156
	v_mov_b32_e32 v58, v156
	v_mov_b32_e32 v59, v156
	v_mov_b32_e32 v52, 0
	v_mov_b32_e32 v53, v156
	v_mov_b32_e32 v54, v156
	v_mov_b32_e32 v55, v156
	v_mov_b32_e32 v64, 0
	v_mov_b32_e32 v65, v156
	v_mov_b32_e32 v66, v156
	v_mov_b32_e32 v67, v156
	v_mov_b32_e32 v36, 0
	v_mov_b32_e32 v37, v156
	v_mov_b32_e32 v38, v156
	v_mov_b32_e32 v39, v156
	v_mov_b32_e32 v40, 0
	v_mov_b32_e32 v41, v156
	v_mov_b32_e32 v42, v156
	v_mov_b32_e32 v43, v156
	v_mov_b32_e32 v44, 0
	v_mov_b32_e32 v45, v156
	v_mov_b32_e32 v46, v156
	v_mov_b32_e32 v47, v156
	v_mov_b32_e32 v48, 0
	v_mov_b32_e32 v49, v156
	v_mov_b32_e32 v50, v156
	v_mov_b32_e32 v51, v156
	s_lshl_b32 s34, s0, 6
	s_cmp_gt_u32 s0, 3
	s_mov_b64 s[2:3], -1
	s_cbranch_scc0 .LBB0_540

; #define LAS __attribute__((address_space(3)))
; __device__ __forceinline__ void mlstm_unit(LAS unsigned char* lds, const bf16_t* __restrict__ PM, const float* __restrict__ GATES, bf16_t* __restrict__ Hout,
;                                            int b, int h, int dir, int vs, Conv& cvs, const int wave_) {
;     ...
;         const bool lat = ci >= 4;
;         const int row0 = ML_ROW0(ci);
; #pragma unroll
;         for (int j = 0; j < 4; ++j) *(LAS u32x4*)(lds + KS + sr * RQ + (j * 8 + c8) * 16) = rk[j];
;         *(LAS u32x4*)(lds + VS + sr * RV + c8 * 16) = rv;
;         if (lat) {
; #pragma unroll
;             for (int j = 0; j < 4; ++j) *(LAS u32x4*)(lds + QS + sr * RQ + (j * 8 + c8) * 16) = rq[j];
;         }
.LBB0_542:
	s_cmp_gt_u32 s0, 3
	s_cselect_b64 s[94:95], -1, 0
	s_cmp_lt_u32 s0, 4
	v_add_u32_e32 v132, v159, v144
	s_mov_b64 vcc, s[92:93]
	s_cbranch_vccnz .Lml_nowait
	s_waitcnt vmcnt(0)
.Lml_nowait:
	ds_write_b128 v132, v[0:3] offset:33792
	ds_write_b128 v132, v[4:7] offset:33920
	ds_write_b128 v132, v[8:11] offset:34048
	ds_write_b128 v132, v[12:15] offset:34176
	ds_write_b128 v182, v[16:19]
	s_cbranch_scc1 .LBB0_544
	ds_write_b128 v183, v[32:35]
	ds_write_b128 v183, v[28:31] offset:128
	ds_write_b128 v183, v[24:27] offset:256
	ds_write_b128 v183, v[20:23] offset:384
